# scan: state waves read KDT/BT/V row-major LDS images with transposed reads, helper store path no longer builds transposed images; helper waves at raised priority; plus earlier helper inverse rewrite
# baseline (speedup 1.0000x reference)
.LBB0_1105:
	s_and_b32 s0, s11, 1
	s_bfe_u32 s8, s11, 0x30001
	s_cmp_eq_u32 s0, 0
	s_cselect_b64 s[6:7], -1, 0
	s_and_b64 s[0:1], s[6:7], exec
	s_mov_b32 s2, 0x44900000
	s_mov_b32 s0, 0x2dc00000
	s_mov_b32 s1, 0x36c00000
	s_cselect_b32 s2, 0x44400000, s2
	s_mul_i32 s3, s8, 0x90000
	s_mov_b32 s4, 0x32400000
	s_mov_b32 s5, 0x3b400000
	s_cselect_b32 s0, 0x2b800000, s0
	s_cselect_b32 s1, 0x34800000, s1
	s_cselect_b32 s4, 0x30000000, s4
	s_cselect_b32 s5, 0x39000000, s5
	s_add_i32 s2, s2, s3
	v_writelane_b32 v255, s2, 11
	v_writelane_b32 v255, s11, 12
	s_ashr_i32 s2, s11, 4
	v_writelane_b32 v255, s2, 13
	v_readlane_b32 s2, v254, 47
	v_readlane_b32 s3, v254, 48
	s_andn2_b64 vcc, exec, s[2:3]
	s_mul_i32 s2, s8, 0x9000
	v_writelane_b32 v255, s2, 14
	v_or_b32_e32 v180, s0, v132
	v_or_b32_e32 v181, s0, v133
	v_or_b32_e32 v182, s5, v132
	v_or_b32_e32 v183, s5, v133
	v_or_b32_e32 v184, s1, v132
	v_or_b32_e32 v185, s1, v133
	v_or_b32_e32 v186, s4, v132
	v_or_b32_e32 v187, s4, v133
	s_barrier
	s_cbranch_vccnz .LBB0_1109
	v_readlane_b32 s0, v255, 13
	s_lshl_b32 s40, s0, 11
	s_addk_i32 s40, 0x1000
	v_cndmask_b32_e64 v2, v95, v94, s[6:7]
	s_lshl_b32 s50, s0, 8
	v_cndmask_b32_e64 v3, v96, v1, s[6:7]
	v_readlane_b32 s0, v254, 37
	v_add_u32_e32 v2, s40, v2
	v_add_u32_e32 v3, s50, v3
	v_readlane_b32 s1, v254, 38
	v_add_u32_e32 v42, v102, v132
	s_nop 0
	v_cndmask_b32_e64 v2, v2, v3, s[0:1]
	s_mul_i32 s0, s8, 0x9000
	v_add_lshl_u32 v2, v2, s0, 7
	v_add_u32_e32 v3, v2, v180
	global_load_dwordx4 v[14:17], v3, s[12:13]
	v_add_u32_e32 v3, v2, v181
	global_load_dwordx4 v[18:21], v3, s[12:13]
	v_add_u32_e32 v3, v2, v182
	global_load_dwordx4 v[22:25], v3, s[12:13]
	v_add_u32_e32 v3, v2, v183
	global_load_dwordx4 v[26:29], v3, s[12:13]
	v_add_u32_e32 v3, v2, v184
	global_load_dwordx4 v[30:33], v3, s[12:13]
	v_add_u32_e32 v3, v2, v185
	global_load_dwordx4 v[34:37], v3, s[12:13]
	v_add_u32_e32 v3, v2, v186
	global_load_dwordx4 v[38:41], v3, s[12:13]
	v_add_u32_e32 v3, v2, v187
	global_load_dwordx4 v[10:13], v3, s[12:13]
	v_add_u32_e32 v3, v2, v134
	global_load_dwordx4 v[6:9], v3, s[12:13]
	v_add_u32_e32 v2, v2, v135
	global_load_dwordx4 v[2:5], v2, s[12:13]
	s_waitcnt vmcnt(9)
	ds_write_b128 v42, v[14:17]
	v_add_u32_e32 v14, v102, v133
	s_waitcnt vmcnt(8)
	ds_write_b128 v14, v[18:21]
	s_waitcnt vmcnt(7)
	ds_write_b128 v42, v[22:25] offset:4608
	s_waitcnt vmcnt(6)
	ds_write_b128 v14, v[26:29] offset:4608
	s_waitcnt vmcnt(5)
	ds_write_b128 v42, v[30:33] offset:9216
	s_waitcnt vmcnt(4)
	ds_write_b128 v14, v[34:37] offset:9216
	s_waitcnt vmcnt(3)
	ds_write_b128 v42, v[38:41] offset:13824
	s_waitcnt vmcnt(2)
	ds_write_b128 v14, v[10:13] offset:13824
	s_waitcnt vmcnt(1)
	ds_write_b128 v42, v[6:9] offset:18432
	s_waitcnt vmcnt(0)
	ds_write_b128 v14, v[2:5] offset:18432
	s_mov_b64 s[30:31], exec
	v_readlane_b32 s0, v254, 41
	v_readlane_b32 s1, v254, 42
	s_and_b64 s[0:1], s[30:31], s[0:1]
	s_mov_b64 exec, s[0:1]
	s_cbranch_execz .LBB0_1108
	v_cndmask_b32_e64 v2, v100, v97, s[6:7]
	v_cndmask_b32_e64 v3, v99, v98, s[6:7]
	v_readlane_b32 s0, v254, 39
	v_add_u32_e32 v2, s50, v2
	v_add_u32_e32 v3, s40, v3
	v_readlane_b32 s1, v254, 40
	s_nop 1
	v_cndmask_b32_e64 v2, v3, v2, s[0:1]
	v_lshlrev_b32_e32 v2, 4, v2
	v_and_b32_e32 v2, 0xffffff00, v2
	v_readlane_b32 s0, v255, 11
	s_nop 1
	v_add_u32_e32 v2, s0, v2
	v_or_b32_e32 v2, v2, v101
	global_load_dwordx4 v[2:5], v2, s[12:13]
	s_waitcnt vmcnt(0)
	ds_write_b128 v170, v[2:5] offset:33792

.LBB0_1114:
	v_writelane_b32 v255, s0, 11
	s_and_b32 s5, s0, 1
	v_readlane_b32 s0, v254, 35
	v_readlane_b32 s1, v254, 36
	s_andn2_b64 vcc, exec, s[0:1]
	s_mov_b64 s[76:77], -1
	v_cndmask_b32_e64 v18, 0, 1, s[0:1]
	v_cmp_ne_u32_e64 s[8:9], 1, v18
	s_mul_i32 s0, s5, 0x1e00
	v_add_u32_e32 v34, v115, v155
	v_writelane_b32 v255, s8, 17
	v_add_u32_e32 v35, v115, v117
	v_add_u32_e32 v193, 0, v113
	v_writelane_b32 v255, s9, 18
	v_add_u32_e32 v36, v115, v156
	v_add_u32_e32 v192, s0, v166
	v_writelane_b32 v255, s5, 13
	v_lshl_add_u32 v191, s5, 13, v165
	s_cbranch_vccnz .LBB0_1116
	v_readlane_b32 s0, v255, 13
	v_add_u32_e32 v246, v115, v155
	s_nop 0
	s_nop 0
	s_mul_i32 s1, s0, 0x1e00
	s_lshl_b32 s0, s0, 13
	v_mov_b32_e32 v251, v113
	v_add_u32_e32 v252, s1, v166
	v_add_u32_e32 v253, s0, v165
	v_add_u32_e32 v247, 0x1200, v246
	v_bfe_u32 v248, v0, 4, 2
	v_mul_u32_u24_e32 v248, 0x240, v248
	v_bfe_u32 v249, v0, 2, 2
	v_mul_u32_u24_e32 v249, 0x90, v249
	v_and_b32_e32 v250, 3, v0
	v_add_u32_e32 v248, v248, v249
	v_lshl_add_u32 v248, v250, 3, v248
	v_bfe_u32 v249, v0, 6, 2
	v_lshl_add_u32 v250, v249, 5, v248
	ds_read2_b64 v[18:21], v246 offset1:4
	ds_read2_b64 v[22:25], v246 offset0:8 offset1:12
	ds_read_b64_tr_b16 v[66:67], v250 offset:18432
	ds_read2_b64 v[68:71], v252 offset1:80
	v_cvt_pk_bf16_f32 v198, v2, v3
	v_cvt_pk_bf16_f32 v199, v4, v5
	v_cvt_pk_bf16_f32 v202, v10, v11
	v_cvt_pk_bf16_f32 v203, v12, v13
	v_cvt_pk_bf16_f32 v200, v6, v7
	v_cvt_pk_bf16_f32 v201, v8, v9
	v_cvt_pk_bf16_f32 v204, v14, v15
	v_cvt_pk_bf16_f32 v205, v16, v17
	ds_read2_b64 v[26:29], v247 offset1:4
	ds_read2_b64 v[30:33], v247 offset0:8 offset1:12
	ds_read2_b64 v[72:75], v252 offset0:160 offset1:240
	s_waitcnt lgkmcnt(6)
	v_mfma_f32_16x16x16_bf16 v[206:209], v[18:19], v[198:199], 0
	s_waitcnt lgkmcnt(5)
	v_mfma_f32_16x16x16_bf16 v[210:213], v[22:23], v[202:203], 0
	ds_read_b64_tr_b16 v[34:35], v248 offset:9216
	ds_read_b64_tr_b16 v[36:37], v248 offset:9248
	ds_read_b64_tr_b16 v[38:39], v248 offset:9280
	ds_read_b64_tr_b16 v[40:41], v248 offset:9312
	v_mfma_f32_16x16x16_bf16 v[206:209], v[20:21], v[200:201], v[206:209]
	v_mfma_f32_16x16x16_bf16 v[210:213], v[24:25], v[204:205], v[210:213]
	ds_read_b64_tr_b16 v[42:43], v248 offset:13824
	ds_read_b64_tr_b16 v[44:45], v248 offset:13856
	ds_read_b64_tr_b16 v[46:47], v248 offset:13888
	ds_read_b64_tr_b16 v[48:49], v248 offset:13920
	s_waitcnt lgkmcnt(12)
	s_waitcnt lgkmcnt(11)
	v_mfma_f32_16x16x16_bf16 v[210:213], v[68:69], v[66:67], v[210:213]
	s_waitcnt lgkmcnt(10)
	v_mfma_f32_16x16x16_bf16 v[214:217], v[26:27], v[198:199], 0
	s_waitcnt lgkmcnt(9)
	v_mfma_f32_16x16x16_bf16 v[218:221], v[30:31], v[202:203], 0
	v_mfma_f32_16x16x16_bf16 v[214:217], v[28:29], v[200:201], v[214:217]
	v_mfma_f32_16x16x16_bf16 v[218:221], v[32:33], v[204:205], v[218:221]
	ds_read_b128 v[50:53], v251 offset:33792
	ds_read_b128 v[54:57], v251 offset:33856
	ds_read_b128 v[58:61], v251 offset:33920
	ds_read_b128 v[62:65], v251 offset:33984
	v_add_u32_e32 v246, 0x900, v246
	ds_read2_b64 v[76:79], v246 offset1:4
	s_waitcnt lgkmcnt(13)
	ds_read2_b64 v[80:83], v246 offset0:8 offset1:12
	v_pk_add_f32 v[206:207], v[206:207], v[210:211]
	v_pk_add_f32 v[208:209], v[208:209], v[212:213]
	v_cvt_pk_bf16_f32 v242, v206, v207
	v_cvt_pk_bf16_f32 v243, v208, v209
	s_waitcnt lgkmcnt(13)
	ds_read_b64_tr_b16 v[84:85], v250 offset:20736
	v_add_u32_e32 v252, 0xf00, v252
	s_waitcnt lgkmcnt(13)
	ds_read2_b64 v[86:89], v252 offset1:80
	v_mfma_f32_16x16x16_bf16 v[238:241], v[74:75], v[242:243], 0
	v_mfma_f32_16x16x16_bf16 v[214:217], v[70:71], v[66:67], v[214:217]
	v_mfma_f32_16x16x16_bf16 v[2:5], v[34:35], v[66:67], v[2:5]
	v_mfma_f32_16x16x16_bf16 v[6:9], v[36:37], v[66:67], v[6:9]
	s_waitcnt lgkmcnt(12)
	v_mfma_f32_16x16x16_bf16 v[10:13], v[38:39], v[66:67], v[10:13]
	v_mfma_f32_16x16x16_bf16 v[14:17], v[40:41], v[66:67], v[14:17]
	ds_read2_b64 v[90:93], v252 offset0:160 offset1:240
	v_add_u32_e32 v247, 0x900, v247
	ds_read2_b64 v[26:29], v247 offset1:4
	s_waitcnt lgkmcnt(13)
	ds_read2_b64 v[30:33], v247 offset0:8 offset1:12
	v_cvt_pk_bf16_f32 v244, -v238, -v239
	v_cvt_pk_bf16_f32 v245, -v240, -v241
	s_waitcnt lgkmcnt(13)
	ds_read_b64_tr_b16 v[34:35], v248 offset:11520
	s_waitcnt lgkmcnt(13)
	ds_read_b64_tr_b16 v[36:37], v248 offset:11552
	s_waitcnt lgkmcnt(13)
	ds_read_b64_tr_b16 v[38:39], v248 offset:11584
	s_waitcnt lgkmcnt(13)
	ds_read_b64_tr_b16 v[40:41], v248 offset:11616
	v_mfma_f32_16x16x16_bf16 v[2:5], v[42:43], v[244:245], v[2:5]
	v_mfma_f32_16x16x16_bf16 v[6:9], v[44:45], v[244:245], v[6:9]
	v_mfma_f32_16x16x16_bf16 v[10:13], v[46:47], v[244:245], v[10:13]
	v_mfma_f32_16x16x16_bf16 v[14:17], v[48:49], v[244:245], v[14:17]
	v_mfma_f32_16x16x16_bf16 v[218:221], v[72:73], v[244:245], v[218:221]
	s_waitcnt lgkmcnt(13)
	ds_read_b64_tr_b16 v[42:43], v248 offset:16128
	s_waitcnt lgkmcnt(13)
	ds_read_b64_tr_b16 v[44:45], v248 offset:16160
	s_waitcnt lgkmcnt(13)
	ds_read_b64_tr_b16 v[46:47], v248 offset:16192
	s_waitcnt lgkmcnt(13)
	ds_read_b64_tr_b16 v[48:49], v248 offset:16224
	v_pk_mul_f32 v[2:3], v[50:51], v[2:3]
	v_pk_mul_f32 v[4:5], v[52:53], v[4:5]
	v_pk_mul_f32 v[6:7], v[54:55], v[6:7]
	v_pk_mul_f32 v[8:9], v[56:57], v[8:9]
	v_pk_mul_f32 v[10:11], v[58:59], v[10:11]
	v_pk_mul_f32 v[12:13], v[60:61], v[12:13]
	v_pk_mul_f32 v[14:15], v[62:63], v[14:15]
	v_pk_mul_f32 v[16:17], v[64:65], v[16:17]
	v_pk_add_f32 v[214:215], v[214:215], v[218:219]
	v_pk_add_f32 v[216:217], v[216:217], v[220:221]
	s_waitcnt lgkmcnt(13)
	ds_write2st64_b32 v253, v214, v215 offset0:0 offset1:1
	s_waitcnt lgkmcnt(13)
	ds_write2st64_b32 v253, v216, v217 offset0:2 offset1:3
	s_waitcnt lgkmcnt(13)
	ds_read_b128 v[50:53], v251 offset:34048
	s_waitcnt lgkmcnt(13)
	ds_read_b128 v[54:57], v251 offset:34112
	s_waitcnt lgkmcnt(13)
	ds_read_b128 v[58:61], v251 offset:34176
	s_waitcnt lgkmcnt(13)
	ds_read_b128 v[62:65], v251 offset:34240
	v_cvt_pk_bf16_f32 v198, v2, v3
	v_cvt_pk_bf16_f32 v199, v4, v5
	v_cvt_pk_bf16_f32 v202, v10, v11
	v_cvt_pk_bf16_f32 v203, v12, v13
	v_cvt_pk_bf16_f32 v200, v6, v7
	v_cvt_pk_bf16_f32 v201, v8, v9
	v_cvt_pk_bf16_f32 v204, v14, v15
	v_cvt_pk_bf16_f32 v205, v16, v17
	v_mfma_f32_16x16x16_bf16 v[206:209], v[76:77], v[198:199], 0
	v_mfma_f32_16x16x16_bf16 v[210:213], v[80:81], v[202:203], 0
	v_mfma_f32_16x16x16_bf16 v[206:209], v[78:79], v[200:201], v[206:209]
	v_mfma_f32_16x16x16_bf16 v[210:213], v[82:83], v[204:205], v[210:213]
	v_mfma_f32_16x16x16_bf16 v[210:213], v[86:87], v[84:85], v[210:213]
	v_mfma_f32_16x16x16_bf16 v[214:217], v[26:27], v[198:199], 0
	v_mfma_f32_16x16x16_bf16 v[218:221], v[30:31], v[202:203], 0
	v_mfma_f32_16x16x16_bf16 v[214:217], v[28:29], v[200:201], v[214:217]
	v_mfma_f32_16x16x16_bf16 v[218:221], v[32:33], v[204:205], v[218:221]
	s_nop 3
	v_pk_add_f32 v[206:207], v[206:207], v[210:211]
	v_pk_add_f32 v[208:209], v[208:209], v[212:213]
	v_cvt_pk_bf16_f32 v242, v206, v207
	v_cvt_pk_bf16_f32 v243, v208, v209
	s_nop 1
	v_mfma_f32_16x16x16_bf16 v[238:241], v[92:93], v[242:243], 0
	v_mfma_f32_16x16x16_bf16 v[214:217], v[88:89], v[84:85], v[214:217]
	s_waitcnt lgkmcnt(12)
	v_mfma_f32_16x16x16_bf16 v[2:5], v[34:35], v[84:85], v[2:5]
	v_mfma_f32_16x16x16_bf16 v[6:9], v[36:37], v[84:85], v[6:9]
	s_waitcnt lgkmcnt(10)
	v_mfma_f32_16x16x16_bf16 v[10:13], v[38:39], v[84:85], v[10:13]
	v_mfma_f32_16x16x16_bf16 v[14:17], v[40:41], v[84:85], v[14:17]
	s_nop 0
	v_cvt_pk_bf16_f32 v244, -v238, -v239
	v_cvt_pk_bf16_f32 v245, -v240, -v241
	s_waitcnt lgkmcnt(8)
	s_nop 0
	v_mfma_f32_16x16x16_bf16 v[2:5], v[42:43], v[244:245], v[2:5]
	v_mfma_f32_16x16x16_bf16 v[6:9], v[44:45], v[244:245], v[6:9]
	s_waitcnt lgkmcnt(6)
	v_mfma_f32_16x16x16_bf16 v[10:13], v[46:47], v[244:245], v[10:13]
	v_mfma_f32_16x16x16_bf16 v[14:17], v[48:49], v[244:245], v[14:17]
	v_mfma_f32_16x16x16_bf16 v[218:221], v[90:91], v[244:245], v[218:221]
	s_waitcnt lgkmcnt(3)
	s_nop 1
	v_pk_mul_f32 v[2:3], v[50:51], v[2:3]
	v_pk_mul_f32 v[4:5], v[52:53], v[4:5]
	s_waitcnt lgkmcnt(2)
	v_pk_mul_f32 v[6:7], v[54:55], v[6:7]
	v_pk_mul_f32 v[8:9], v[56:57], v[8:9]
	s_waitcnt lgkmcnt(1)
	v_pk_mul_f32 v[10:11], v[58:59], v[10:11]
	v_pk_mul_f32 v[12:13], v[60:61], v[12:13]
	s_waitcnt lgkmcnt(0)
	v_pk_mul_f32 v[14:15], v[62:63], v[14:15]
	v_pk_mul_f32 v[16:17], v[64:65], v[16:17]
	v_pk_add_f32 v[214:215], v[214:215], v[218:219]
	v_pk_add_f32 v[216:217], v[216:217], v[220:221]
	ds_write2st64_b32 v253, v214, v215 offset0:16 offset1:17
	ds_write2st64_b32 v253, v216, v217 offset0:18 offset1:19
	s_branch .Lscan_join1
.LBB0_1116:
	s_andn2_b64 vcc, exec, s[76:77]
	s_cbranch_vccnz .LBB0_1139
	v_readlane_b32 s0, v255, 13
	s_cmp_lg_u32 s16, s0
	s_mov_b64 s[76:77], -1
	s_cbranch_scc0 .LBB0_1121
	s_setprio 3
	v_writelane_b32 v255, s4, 24
	ds_read_b128 v[18:21], v179 offset:34304
	ds_read_b128 v[26:29], v179 offset:48128
	ds_read_b128 v[22:25], v179 offset:34368
	ds_read_b128 v[30:33], v179 offset:48192
	v_readlane_b32 s0, v255, 13
	v_readlane_b32 s2, v254, 55
	v_readlane_b32 s3, v254, 56
	v_readlane_b32 s4, v254, 57
	v_readlane_b32 s5, v254, 58
	v_readlane_b32 s6, v254, 63
	v_readlane_b32 s7, v255, 0
	s_xor_b32 s0, s0, 1
	s_mulk_i32 s0, 0x1e00
	v_readlane_b32 s8, v255, 1
	v_readlane_b32 s9, v255, 2
	v_readlane_b32 s10, v255, 3
	v_readlane_b32 s11, v255, 4
	v_and_b32_e32 v46, 15, v0
	v_bfe_u32 v47, v0, 4, 2
	v_mad_u32_u24 v194, v46, 38, v114
	v_lshl_add_u32 v194, v47, 3, v194
	v_add_u32_e32 v194, s0, v194
	v_mad_u32_u24 v196, v46, 40, v194
	v_lshl_add_u32 v196, v47, 3, v196
	s_waitcnt lgkmcnt(2)
	v_mfma_f32_16x16x32_bf16 v[38:41], v[26:29], v[18:21], 0
	s_waitcnt lgkmcnt(0)
	v_mfma_f32_16x16x32_bf16 v[38:41], v[30:33], v[22:25], v[38:41]
	ds_read_b128 v[26:29], v179 offset:43520
	ds_read_b128 v[30:33], v179 offset:43584
	v_cndmask_b32_e64 v48, 0, 1.0, s[6:7]
	v_cndmask_b32_e64 v49, 0, 1.0, s[8:9]
	v_cndmask_b32_e64 v46, 1.0, 0, s[2:3]
	v_cndmask_b32_e64 v47, 0, 1.0, s[4:5]
	v_cndmask_b32_e64 v48, v48, 0, s[8:9]
	v_cndmask_b32_e64 v49, v49, 0, s[10:11]
	v_cndmask_b32_e64 v46, v46, 0, s[4:5]
	v_cndmask_b32_e64 v47, v47, 0, s[6:7]
	v_cndmask_b32_e64 v38, 0, v38, s[4:5]
	v_cndmask_b32_e64 v39, 0, v39, s[6:7]
	v_cndmask_b32_e64 v40, 0, v40, s[8:9]
	v_cndmask_b32_e64 v41, 0, v41, s[10:11]
	ds_write_b128 v196, v[38:41] offset:2560
	s_waitcnt lgkmcnt(1)
	v_mfma_f32_16x16x32_bf16 v[42:45], v[26:29], v[18:21], 0
	v_mfma_f32_16x16x32_bf16 v[42:45], v[30:33], v[22:25], v[42:45]
	ds_read_b128 v[18:21], v179 offset:38912
	ds_read_b128 v[22:25], v179 offset:38976
	v_bfe_u32 v38, v0, 4, 2
	v_lshlrev_b32_e32 v38, 4, v38
	v_sub_u32_e32 v196, v196, v38
	s_nop 4
	v_cndmask_b32_e64 v42, 0, v42, s[4:5]
	v_cndmask_b32_e64 v43, 0, v43, s[6:7]
	v_cndmask_b32_e64 v44, 0, v44, s[8:9]
	v_cndmask_b32_e64 v45, 0, v45, s[10:11]
	v_cvt_pk_bf16_f32 v42, v42, v43
	v_cvt_pk_bf16_f32 v43, v44, v45
	ds_write_b64 v194, v[42:43]
	s_waitcnt lgkmcnt(1)
	v_mfma_f32_16x16x32_bf16 v[38:41], v[26:29], v[18:21], 0
	v_mfma_f32_16x16x32_bf16 v[38:41], v[30:33], v[22:25], v[38:41]
	ds_read_b128 v[26:29], v179 offset:48128
	ds_read_b128 v[30:33], v179 offset:48192
	s_waitcnt lgkmcnt(0)
	v_mfma_f32_16x16x32_bf16 v[42:45], v[26:29], v[18:21], 0
	v_mfma_f32_16x16x32_bf16 v[42:45], v[30:33], v[22:25], v[42:45]
	ds_read_b128 v[18:21], v196 offset:2560
	ds_read_b128 v[22:25], v196 offset:2576
	ds_read_b128 v[26:29], v196 offset:2592
	ds_read_b128 v[30:33], v196 offset:2608
	v_cndmask_b32_e64 v38, v38, 0, s[2:3]
	v_cndmask_b32_e64 v39, 0, v39, s[4:5]
	v_cndmask_b32_e64 v40, 0, v40, s[6:7]
	v_cndmask_b32_e64 v41, 0, v41, s[8:9]
	v_cvt_pk_bf16_f32 v38, v38, v39
	v_cvt_pk_bf16_f32 v39, v40, v41
	ds_write_b64 v194, v[38:39] offset:640
	v_cndmask_b32_e64 v42, v42, 0, s[2:3]
	v_cndmask_b32_e64 v43, 0, v43, s[4:5]
	v_cndmask_b32_e64 v44, 0, v44, s[6:7]
	v_cndmask_b32_e64 v45, 0, v45, s[8:9]
	v_cvt_pk_bf16_f32 v42, v42, v43
	v_cvt_pk_bf16_f32 v43, v44, v45
	ds_write_b64 v194, v[42:43] offset:1280
	s_waitcnt lgkmcnt(2)
	v_fmac_f32_dpp v46, v46, -v18 row_newbcast:0 row_mask:0xf bank_mask:0xf
	s_nop 1
	v_fmac_f32_dpp v46, v46, -v19 row_newbcast:1 row_mask:0xf bank_mask:0xf
	v_fmac_f32_dpp v47, v47, -v19 row_newbcast:1 row_mask:0xf bank_mask:0xf
	s_nop 0
	v_fmac_f32_dpp v46, v46, -v20 row_newbcast:2 row_mask:0xf bank_mask:0xf
	v_fmac_f32_dpp v47, v47, -v20 row_newbcast:2 row_mask:0xf bank_mask:0xf
	v_fmac_f32_dpp v48, v48, -v20 row_newbcast:2 row_mask:0xf bank_mask:0xf
	v_fmac_f32_dpp v46, v46, -v21 row_newbcast:3 row_mask:0xf bank_mask:0xf
	v_fmac_f32_dpp v47, v47, -v21 row_newbcast:3 row_mask:0xf bank_mask:0xf
	v_fmac_f32_dpp v48, v48, -v21 row_newbcast:3 row_mask:0xf bank_mask:0xf
	v_fmac_f32_dpp v49, v49, -v21 row_newbcast:3 row_mask:0xf bank_mask:0xf
	v_fmac_f32_dpp v46, v46, -v22 row_newbcast:4 row_mask:0xf bank_mask:0xf
	v_fmac_f32_dpp v47, v47, -v22 row_newbcast:4 row_mask:0xf bank_mask:0xf
	v_fmac_f32_dpp v48, v48, -v22 row_newbcast:4 row_mask:0xf bank_mask:0xf
	v_fmac_f32_dpp v49, v49, -v22 row_newbcast:4 row_mask:0xf bank_mask:0xf
	v_fmac_f32_dpp v46, v46, -v23 row_newbcast:5 row_mask:0xf bank_mask:0xf
	v_fmac_f32_dpp v47, v47, -v23 row_newbcast:5 row_mask:0xf bank_mask:0xf
	v_fmac_f32_dpp v48, v48, -v23 row_newbcast:5 row_mask:0xf bank_mask:0xf
	v_fmac_f32_dpp v49, v49, -v23 row_newbcast:5 row_mask:0xf bank_mask:0xf
	v_fmac_f32_dpp v46, v46, -v24 row_newbcast:6 row_mask:0xf bank_mask:0xf
	v_fmac_f32_dpp v47, v47, -v24 row_newbcast:6 row_mask:0xf bank_mask:0xf
	v_fmac_f32_dpp v48, v48, -v24 row_newbcast:6 row_mask:0xf bank_mask:0xf
	v_fmac_f32_dpp v49, v49, -v24 row_newbcast:6 row_mask:0xf bank_mask:0xf
	v_fmac_f32_dpp v46, v46, -v25 row_newbcast:7 row_mask:0xf bank_mask:0xf
	v_fmac_f32_dpp v47, v47, -v25 row_newbcast:7 row_mask:0xf bank_mask:0xf
	v_fmac_f32_dpp v48, v48, -v25 row_newbcast:7 row_mask:0xf bank_mask:0xf
	v_fmac_f32_dpp v49, v49, -v25 row_newbcast:7 row_mask:0xf bank_mask:0xf
	v_fmac_f32_dpp v46, v46, -v26 row_newbcast:8 row_mask:0xf bank_mask:0xf
	v_fmac_f32_dpp v47, v47, -v26 row_newbcast:8 row_mask:0xf bank_mask:0xf
	v_fmac_f32_dpp v48, v48, -v26 row_newbcast:8 row_mask:0xf bank_mask:0xf
	v_fmac_f32_dpp v49, v49, -v26 row_newbcast:8 row_mask:0xf bank_mask:0xf
	v_fmac_f32_dpp v46, v46, -v27 row_newbcast:9 row_mask:0xf bank_mask:0xf
	v_fmac_f32_dpp v47, v47, -v27 row_newbcast:9 row_mask:0xf bank_mask:0xf
	v_fmac_f32_dpp v48, v48, -v27 row_newbcast:9 row_mask:0xf bank_mask:0xf
	v_fmac_f32_dpp v49, v49, -v27 row_newbcast:9 row_mask:0xf bank_mask:0xf
	v_fmac_f32_dpp v46, v46, -v28 row_newbcast:10 row_mask:0xf bank_mask:0xf
	v_fmac_f32_dpp v47, v47, -v28 row_newbcast:10 row_mask:0xf bank_mask:0xf
	v_fmac_f32_dpp v48, v48, -v28 row_newbcast:10 row_mask:0xf bank_mask:0xf
	v_fmac_f32_dpp v49, v49, -v28 row_newbcast:10 row_mask:0xf bank_mask:0xf
	v_fmac_f32_dpp v46, v46, -v29 row_newbcast:11 row_mask:0xf bank_mask:0xf
	v_fmac_f32_dpp v47, v47, -v29 row_newbcast:11 row_mask:0xf bank_mask:0xf
	v_fmac_f32_dpp v48, v48, -v29 row_newbcast:11 row_mask:0xf bank_mask:0xf
	v_fmac_f32_dpp v49, v49, -v29 row_newbcast:11 row_mask:0xf bank_mask:0xf
	v_fmac_f32_dpp v46, v46, -v30 row_newbcast:12 row_mask:0xf bank_mask:0xf
	v_fmac_f32_dpp v47, v47, -v30 row_newbcast:12 row_mask:0xf bank_mask:0xf
	v_fmac_f32_dpp v48, v48, -v30 row_newbcast:12 row_mask:0xf bank_mask:0xf
	v_fmac_f32_dpp v49, v49, -v30 row_newbcast:12 row_mask:0xf bank_mask:0xf
	v_fmac_f32_dpp v46, v46, -v31 row_newbcast:13 row_mask:0xf bank_mask:0xf
	v_fmac_f32_dpp v47, v47, -v31 row_newbcast:13 row_mask:0xf bank_mask:0xf
	v_fmac_f32_dpp v48, v48, -v31 row_newbcast:13 row_mask:0xf bank_mask:0xf
	v_fmac_f32_dpp v49, v49, -v31 row_newbcast:13 row_mask:0xf bank_mask:0xf
	v_fmac_f32_dpp v46, v46, -v32 row_newbcast:14 row_mask:0xf bank_mask:0xf
	v_fmac_f32_dpp v47, v47, -v32 row_newbcast:14 row_mask:0xf bank_mask:0xf
	v_fmac_f32_dpp v48, v48, -v32 row_newbcast:14 row_mask:0xf bank_mask:0xf
	v_fmac_f32_dpp v49, v49, -v32 row_newbcast:14 row_mask:0xf bank_mask:0xf
	v_cvt_pk_bf16_f32 v46, v46, v47
	v_cvt_pk_bf16_f32 v47, v48, v49
	ds_write_b64 v194, v[46:47] offset:1920
	s_mov_b64 s[76:77], exec

.LBB0_1121:
	s_andn2_b64 vcc, exec, s[76:77]
	s_cbranch_vccnz .LBB0_1138
	s_setprio 3
	v_add_u32_e32 v18, v118, v132
	s_waitcnt vmcnt(6)
	v_add_u32_e32 v19, v118, v133
	ds_write_b128 v18, v[82:85]
	ds_write_b128 v19, v[78:81]
	ds_write_b128 v18, v[90:93] offset:4608
	ds_write_b128 v19, v[86:89] offset:4608
	ds_write_b128 v18, v[74:77] offset:9216
	s_waitcnt vmcnt(5)
	ds_write_b128 v19, v[70:73] offset:9216
	s_waitcnt vmcnt(4)
	ds_write_b128 v18, v[66:69] offset:13824
	s_waitcnt vmcnt(3)
	ds_write_b128 v19, v[58:61] offset:13824
	s_waitcnt vmcnt(2)
	ds_write_b128 v18, v[54:57] offset:18432
	s_waitcnt vmcnt(1)
	ds_write_b128 v19, v[50:53] offset:18432
	s_mov_b64 s[76:77], exec
	v_readlane_b32 s0, v254, 41
	v_readlane_b32 s1, v254, 42
	s_and_b64 s[0:1], s[76:77], s[0:1]
	s_mov_b64 exec, s[0:1]
	s_cbranch_execz .LBB0_1124
	s_waitcnt vmcnt(0)
	ds_write_b128 v173, v[62:65]

.LBB0_1140:
.Lscan_join1:
	s_waitcnt lgkmcnt(0)
	s_barrier
	v_readlane_b32 s0, v255, 17
	v_readlane_b32 s1, v255, 18
	s_and_b64 vcc, exec, s[0:1]
	s_mov_b64 s[76:77], -1
	s_cbranch_vccnz .LBB0_1142
	v_readlane_b32 s0, v255, 13
	v_add_u32_e32 v246, v115, v155
	s_nop 0
	s_xor_b32 s0, s0, 1
	s_mul_i32 s1, s0, 0x1e00
	s_lshl_b32 s0, s0, 13
	v_add_u32_e32 v246, 0x8600, v246
	v_add_u32_e32 v251, 0x8600, v113
	v_add_u32_e32 v252, s1, v166
	v_add_u32_e32 v253, s0, v165
	v_add_u32_e32 v247, 0x1200, v246
	v_bfe_u32 v248, v0, 4, 2
	v_mul_u32_u24_e32 v248, 0x240, v248
	v_bfe_u32 v249, v0, 2, 2
	v_mul_u32_u24_e32 v249, 0x90, v249
	v_and_b32_e32 v250, 3, v0
	v_add_u32_e32 v248, v248, v249
	v_lshl_add_u32 v248, v250, 3, v248
	v_add_u32_e32 v248, 0x8600, v248
	v_bfe_u32 v249, v0, 6, 2
	v_lshl_add_u32 v250, v249, 5, v248
	ds_read2_b64 v[18:21], v246 offset1:4
	ds_read2_b64 v[22:25], v246 offset0:8 offset1:12
	ds_read_b64_tr_b16 v[66:67], v250 offset:18432
	ds_read2_b64 v[68:71], v252 offset1:80
	v_cvt_pk_bf16_f32 v198, v2, v3
	v_cvt_pk_bf16_f32 v199, v4, v5
	v_cvt_pk_bf16_f32 v202, v10, v11
	v_cvt_pk_bf16_f32 v203, v12, v13
	v_cvt_pk_bf16_f32 v200, v6, v7
	v_cvt_pk_bf16_f32 v201, v8, v9
	v_cvt_pk_bf16_f32 v204, v14, v15
	v_cvt_pk_bf16_f32 v205, v16, v17
	ds_read2_b64 v[26:29], v247 offset1:4
	ds_read2_b64 v[30:33], v247 offset0:8 offset1:12
	ds_read2_b64 v[72:75], v252 offset0:160 offset1:240
	s_waitcnt lgkmcnt(6)
	v_mfma_f32_16x16x16_bf16 v[206:209], v[18:19], v[198:199], 0
	s_waitcnt lgkmcnt(5)
	v_mfma_f32_16x16x16_bf16 v[210:213], v[22:23], v[202:203], 0
	ds_read_b64_tr_b16 v[34:35], v248 offset:9216
	ds_read_b64_tr_b16 v[36:37], v248 offset:9248
	ds_read_b64_tr_b16 v[38:39], v248 offset:9280
	ds_read_b64_tr_b16 v[40:41], v248 offset:9312
	v_mfma_f32_16x16x16_bf16 v[206:209], v[20:21], v[200:201], v[206:209]
	v_mfma_f32_16x16x16_bf16 v[210:213], v[24:25], v[204:205], v[210:213]
	ds_read_b64_tr_b16 v[42:43], v248 offset:13824
	ds_read_b64_tr_b16 v[44:45], v248 offset:13856
	ds_read_b64_tr_b16 v[46:47], v248 offset:13888
	ds_read_b64_tr_b16 v[48:49], v248 offset:13920
	s_waitcnt lgkmcnt(12)
	s_waitcnt lgkmcnt(11)
	v_mfma_f32_16x16x16_bf16 v[210:213], v[68:69], v[66:67], v[210:213]
	s_waitcnt lgkmcnt(10)
	v_mfma_f32_16x16x16_bf16 v[214:217], v[26:27], v[198:199], 0
	s_waitcnt lgkmcnt(9)
	v_mfma_f32_16x16x16_bf16 v[218:221], v[30:31], v[202:203], 0
	v_mfma_f32_16x16x16_bf16 v[214:217], v[28:29], v[200:201], v[214:217]
	v_mfma_f32_16x16x16_bf16 v[218:221], v[32:33], v[204:205], v[218:221]
	ds_read_b128 v[50:53], v251 offset:33792
	ds_read_b128 v[54:57], v251 offset:33856
	ds_read_b128 v[58:61], v251 offset:33920
	ds_read_b128 v[62:65], v251 offset:33984
	v_add_u32_e32 v246, 0x900, v246
	ds_read2_b64 v[76:79], v246 offset1:4
	s_waitcnt lgkmcnt(13)
	ds_read2_b64 v[80:83], v246 offset0:8 offset1:12
	v_pk_add_f32 v[206:207], v[206:207], v[210:211]
	v_pk_add_f32 v[208:209], v[208:209], v[212:213]
	v_cvt_pk_bf16_f32 v242, v206, v207
	v_cvt_pk_bf16_f32 v243, v208, v209
	s_waitcnt lgkmcnt(13)
	ds_read_b64_tr_b16 v[84:85], v250 offset:20736
	v_add_u32_e32 v252, 0xf00, v252
	s_waitcnt lgkmcnt(13)
	ds_read2_b64 v[86:89], v252 offset1:80
	v_mfma_f32_16x16x16_bf16 v[238:241], v[74:75], v[242:243], 0
	v_mfma_f32_16x16x16_bf16 v[214:217], v[70:71], v[66:67], v[214:217]
	v_mfma_f32_16x16x16_bf16 v[2:5], v[34:35], v[66:67], v[2:5]
	v_mfma_f32_16x16x16_bf16 v[6:9], v[36:37], v[66:67], v[6:9]
	s_waitcnt lgkmcnt(12)
	v_mfma_f32_16x16x16_bf16 v[10:13], v[38:39], v[66:67], v[10:13]
	v_mfma_f32_16x16x16_bf16 v[14:17], v[40:41], v[66:67], v[14:17]
	ds_read2_b64 v[90:93], v252 offset0:160 offset1:240
	v_add_u32_e32 v247, 0x900, v247
	ds_read2_b64 v[26:29], v247 offset1:4
	s_waitcnt lgkmcnt(13)
	ds_read2_b64 v[30:33], v247 offset0:8 offset1:12
	v_cvt_pk_bf16_f32 v244, -v238, -v239
	v_cvt_pk_bf16_f32 v245, -v240, -v241
	s_waitcnt lgkmcnt(13)
	ds_read_b64_tr_b16 v[34:35], v248 offset:11520
	s_waitcnt lgkmcnt(13)
	ds_read_b64_tr_b16 v[36:37], v248 offset:11552
	s_waitcnt lgkmcnt(13)
	ds_read_b64_tr_b16 v[38:39], v248 offset:11584
	s_waitcnt lgkmcnt(13)
	ds_read_b64_tr_b16 v[40:41], v248 offset:11616
	v_mfma_f32_16x16x16_bf16 v[2:5], v[42:43], v[244:245], v[2:5]
	v_mfma_f32_16x16x16_bf16 v[6:9], v[44:45], v[244:245], v[6:9]
	v_mfma_f32_16x16x16_bf16 v[10:13], v[46:47], v[244:245], v[10:13]
	v_mfma_f32_16x16x16_bf16 v[14:17], v[48:49], v[244:245], v[14:17]
	v_mfma_f32_16x16x16_bf16 v[218:221], v[72:73], v[244:245], v[218:221]
	s_waitcnt lgkmcnt(13)
	ds_read_b64_tr_b16 v[42:43], v248 offset:16128
	s_waitcnt lgkmcnt(13)
	ds_read_b64_tr_b16 v[44:45], v248 offset:16160
	s_waitcnt lgkmcnt(13)
	ds_read_b64_tr_b16 v[46:47], v248 offset:16192
	s_waitcnt lgkmcnt(13)
	ds_read_b64_tr_b16 v[48:49], v248 offset:16224
	v_pk_mul_f32 v[2:3], v[50:51], v[2:3]
	v_pk_mul_f32 v[4:5], v[52:53], v[4:5]
	v_pk_mul_f32 v[6:7], v[54:55], v[6:7]
	v_pk_mul_f32 v[8:9], v[56:57], v[8:9]
	v_pk_mul_f32 v[10:11], v[58:59], v[10:11]
	v_pk_mul_f32 v[12:13], v[60:61], v[12:13]
	v_pk_mul_f32 v[14:15], v[62:63], v[14:15]
	v_pk_mul_f32 v[16:17], v[64:65], v[16:17]
	v_pk_add_f32 v[214:215], v[214:215], v[218:219]
	v_pk_add_f32 v[216:217], v[216:217], v[220:221]
	s_waitcnt lgkmcnt(13)
	ds_write2st64_b32 v253, v214, v215 offset0:0 offset1:1
	s_waitcnt lgkmcnt(13)
	ds_write2st64_b32 v253, v216, v217 offset0:2 offset1:3
	s_waitcnt lgkmcnt(13)
	ds_read_b128 v[50:53], v251 offset:34048
	s_waitcnt lgkmcnt(13)
	ds_read_b128 v[54:57], v251 offset:34112
	s_waitcnt lgkmcnt(13)
	ds_read_b128 v[58:61], v251 offset:34176
	s_waitcnt lgkmcnt(13)
	ds_read_b128 v[62:65], v251 offset:34240
	v_cvt_pk_bf16_f32 v198, v2, v3
	v_cvt_pk_bf16_f32 v199, v4, v5
	v_cvt_pk_bf16_f32 v202, v10, v11
	v_cvt_pk_bf16_f32 v203, v12, v13
	v_cvt_pk_bf16_f32 v200, v6, v7
	v_cvt_pk_bf16_f32 v201, v8, v9
	v_cvt_pk_bf16_f32 v204, v14, v15
	v_cvt_pk_bf16_f32 v205, v16, v17
	v_mfma_f32_16x16x16_bf16 v[206:209], v[76:77], v[198:199], 0
	v_mfma_f32_16x16x16_bf16 v[210:213], v[80:81], v[202:203], 0
	v_mfma_f32_16x16x16_bf16 v[206:209], v[78:79], v[200:201], v[206:209]
	v_mfma_f32_16x16x16_bf16 v[210:213], v[82:83], v[204:205], v[210:213]
	v_mfma_f32_16x16x16_bf16 v[210:213], v[86:87], v[84:85], v[210:213]
	v_mfma_f32_16x16x16_bf16 v[214:217], v[26:27], v[198:199], 0
	v_mfma_f32_16x16x16_bf16 v[218:221], v[30:31], v[202:203], 0
	v_mfma_f32_16x16x16_bf16 v[214:217], v[28:29], v[200:201], v[214:217]
	v_mfma_f32_16x16x16_bf16 v[218:221], v[32:33], v[204:205], v[218:221]
	s_nop 3
	v_pk_add_f32 v[206:207], v[206:207], v[210:211]
	v_pk_add_f32 v[208:209], v[208:209], v[212:213]
	v_cvt_pk_bf16_f32 v242, v206, v207
	v_cvt_pk_bf16_f32 v243, v208, v209
	s_nop 1
	v_mfma_f32_16x16x16_bf16 v[238:241], v[92:93], v[242:243], 0
	v_mfma_f32_16x16x16_bf16 v[214:217], v[88:89], v[84:85], v[214:217]
	s_waitcnt lgkmcnt(12)
	v_mfma_f32_16x16x16_bf16 v[2:5], v[34:35], v[84:85], v[2:5]
	v_mfma_f32_16x16x16_bf16 v[6:9], v[36:37], v[84:85], v[6:9]
	s_waitcnt lgkmcnt(10)
	v_mfma_f32_16x16x16_bf16 v[10:13], v[38:39], v[84:85], v[10:13]
	v_mfma_f32_16x16x16_bf16 v[14:17], v[40:41], v[84:85], v[14:17]
	s_nop 0
	v_cvt_pk_bf16_f32 v244, -v238, -v239
	v_cvt_pk_bf16_f32 v245, -v240, -v241
	s_waitcnt lgkmcnt(8)
	s_nop 0
	v_mfma_f32_16x16x16_bf16 v[2:5], v[42:43], v[244:245], v[2:5]
	v_mfma_f32_16x16x16_bf16 v[6:9], v[44:45], v[244:245], v[6:9]
	s_waitcnt lgkmcnt(6)
	v_mfma_f32_16x16x16_bf16 v[10:13], v[46:47], v[244:245], v[10:13]
	v_mfma_f32_16x16x16_bf16 v[14:17], v[48:49], v[244:245], v[14:17]
	v_mfma_f32_16x16x16_bf16 v[218:221], v[90:91], v[244:245], v[218:221]
	s_waitcnt lgkmcnt(3)
	s_nop 1
	v_pk_mul_f32 v[2:3], v[50:51], v[2:3]
	v_pk_mul_f32 v[4:5], v[52:53], v[4:5]
	s_waitcnt lgkmcnt(2)
	v_pk_mul_f32 v[6:7], v[54:55], v[6:7]
	v_pk_mul_f32 v[8:9], v[56:57], v[8:9]
	s_waitcnt lgkmcnt(1)
	v_pk_mul_f32 v[10:11], v[58:59], v[10:11]
	v_pk_mul_f32 v[12:13], v[60:61], v[12:13]
	s_waitcnt lgkmcnt(0)
	v_pk_mul_f32 v[14:15], v[62:63], v[14:15]
	v_pk_mul_f32 v[16:17], v[64:65], v[16:17]
	v_pk_add_f32 v[214:215], v[214:215], v[218:219]
	v_pk_add_f32 v[216:217], v[216:217], v[220:221]
	ds_write2st64_b32 v253, v214, v215 offset0:16 offset1:17
	ds_write2st64_b32 v253, v216, v217 offset0:18 offset1:19
	s_branch .Lscan_join2
.LBB0_1142:
	s_andn2_b64 vcc, exec, s[76:77]
	s_cbranch_vccnz .LBB0_1159
	v_readlane_b32 s0, v255, 13
	s_xor_b32 s0, s0, s16
	s_cmp_lg_u32 s0, 1
	s_mov_b64 s[76:77], -1
	s_cbranch_scc0 .LBB0_1147
	s_setprio 3
	v_writelane_b32 v255, s4, 24
	v_add_u32_e32 v211, 0x10c00, v179
	ds_read_b128 v[34:37], v211 offset:0
	ds_read_b128 v[42:45], v211 offset:13824
	ds_read_b128 v[38:41], v211 offset:64
	ds_read_b128 v[46:49], v211 offset:13888
	v_readlane_b32 s0, v255, 11
	v_readlane_b32 s2, v254, 55
	v_readlane_b32 s3, v254, 56
	v_readlane_b32 s4, v254, 57
	v_readlane_b32 s5, v254, 58
	v_readlane_b32 s6, v254, 63
	v_readlane_b32 s7, v255, 0
	s_bitcmp1_b32 s0, 0
	s_cselect_b32 s0, 0x1e00, 0
	v_readlane_b32 s8, v255, 1
	v_readlane_b32 s9, v255, 2
	v_readlane_b32 s10, v255, 3
	v_readlane_b32 s11, v255, 4
	v_and_b32_e32 v206, 15, v0
	v_bfe_u32 v207, v0, 4, 2
	v_mad_u32_u24 v194, v206, 38, v114
	v_lshl_add_u32 v194, v207, 3, v194
	v_add_u32_e32 v194, s0, v194
	v_mad_u32_u24 v196, v206, 40, v194
	v_lshl_add_u32 v196, v207, 3, v196
	s_waitcnt lgkmcnt(2)
	v_mfma_f32_16x16x32_bf16 v[198:201], v[42:45], v[34:37], 0
	s_waitcnt lgkmcnt(0)
	v_mfma_f32_16x16x32_bf16 v[198:201], v[46:49], v[38:41], v[198:201]
	ds_read_b128 v[42:45], v211 offset:9216
	ds_read_b128 v[46:49], v211 offset:9280
	v_cndmask_b32_e64 v208, 0, 1.0, s[6:7]
	v_cndmask_b32_e64 v209, 0, 1.0, s[8:9]
	v_cndmask_b32_e64 v206, 1.0, 0, s[2:3]
	v_cndmask_b32_e64 v207, 0, 1.0, s[4:5]
	v_cndmask_b32_e64 v208, v208, 0, s[8:9]
	v_cndmask_b32_e64 v209, v209, 0, s[10:11]
	v_cndmask_b32_e64 v206, v206, 0, s[4:5]
	v_cndmask_b32_e64 v207, v207, 0, s[6:7]
	v_cndmask_b32_e64 v198, 0, v198, s[4:5]
	v_cndmask_b32_e64 v199, 0, v199, s[6:7]
	v_cndmask_b32_e64 v200, 0, v200, s[8:9]
	v_cndmask_b32_e64 v201, 0, v201, s[10:11]
	ds_write_b128 v196, v[198:201] offset:2560
	s_waitcnt lgkmcnt(1)
	v_mfma_f32_16x16x32_bf16 v[202:205], v[42:45], v[34:37], 0
	v_mfma_f32_16x16x32_bf16 v[202:205], v[46:49], v[38:41], v[202:205]
	ds_read_b128 v[34:37], v211 offset:4608
	ds_read_b128 v[38:41], v211 offset:4672
	v_bfe_u32 v198, v0, 4, 2
	v_lshlrev_b32_e32 v198, 4, v198
	v_sub_u32_e32 v196, v196, v198
	s_nop 4
	v_cndmask_b32_e64 v202, 0, v202, s[4:5]
	v_cndmask_b32_e64 v203, 0, v203, s[6:7]
	v_cndmask_b32_e64 v204, 0, v204, s[8:9]
	v_cndmask_b32_e64 v205, 0, v205, s[10:11]
	v_cvt_pk_bf16_f32 v202, v202, v203
	v_cvt_pk_bf16_f32 v203, v204, v205
	ds_write_b64 v194, v[202:203]
	s_waitcnt lgkmcnt(1)
	v_mfma_f32_16x16x32_bf16 v[198:201], v[42:45], v[34:37], 0
	v_mfma_f32_16x16x32_bf16 v[198:201], v[46:49], v[38:41], v[198:201]
	ds_read_b128 v[42:45], v211 offset:13824
	ds_read_b128 v[46:49], v211 offset:13888
	s_waitcnt lgkmcnt(0)
	v_mfma_f32_16x16x32_bf16 v[202:205], v[42:45], v[34:37], 0
	v_mfma_f32_16x16x32_bf16 v[202:205], v[46:49], v[38:41], v[202:205]
	ds_read_b128 v[34:37], v196 offset:2560
	ds_read_b128 v[38:41], v196 offset:2576
	ds_read_b128 v[42:45], v196 offset:2592
	ds_read_b128 v[46:49], v196 offset:2608
	v_cndmask_b32_e64 v198, v198, 0, s[2:3]
	v_cndmask_b32_e64 v199, 0, v199, s[4:5]
	v_cndmask_b32_e64 v200, 0, v200, s[6:7]
	v_cndmask_b32_e64 v201, 0, v201, s[8:9]
	v_cvt_pk_bf16_f32 v198, v198, v199
	v_cvt_pk_bf16_f32 v199, v200, v201
	ds_write_b64 v194, v[198:199] offset:640
	v_cndmask_b32_e64 v202, v202, 0, s[2:3]
	v_cndmask_b32_e64 v203, 0, v203, s[4:5]
	v_cndmask_b32_e64 v204, 0, v204, s[6:7]
	v_cndmask_b32_e64 v205, 0, v205, s[8:9]
	v_cvt_pk_bf16_f32 v202, v202, v203
	v_cvt_pk_bf16_f32 v203, v204, v205
	ds_write_b64 v194, v[202:203] offset:1280
	s_waitcnt lgkmcnt(2)
	v_fmac_f32_dpp v206, v206, -v34 row_newbcast:0 row_mask:0xf bank_mask:0xf
	s_nop 1
	v_fmac_f32_dpp v206, v206, -v35 row_newbcast:1 row_mask:0xf bank_mask:0xf
	v_fmac_f32_dpp v207, v207, -v35 row_newbcast:1 row_mask:0xf bank_mask:0xf
	s_nop 0
	v_fmac_f32_dpp v206, v206, -v36 row_newbcast:2 row_mask:0xf bank_mask:0xf
	v_fmac_f32_dpp v207, v207, -v36 row_newbcast:2 row_mask:0xf bank_mask:0xf
	v_fmac_f32_dpp v208, v208, -v36 row_newbcast:2 row_mask:0xf bank_mask:0xf
	v_fmac_f32_dpp v206, v206, -v37 row_newbcast:3 row_mask:0xf bank_mask:0xf
	v_fmac_f32_dpp v207, v207, -v37 row_newbcast:3 row_mask:0xf bank_mask:0xf
	v_fmac_f32_dpp v208, v208, -v37 row_newbcast:3 row_mask:0xf bank_mask:0xf
	v_fmac_f32_dpp v209, v209, -v37 row_newbcast:3 row_mask:0xf bank_mask:0xf
	v_fmac_f32_dpp v206, v206, -v38 row_newbcast:4 row_mask:0xf bank_mask:0xf
	v_fmac_f32_dpp v207, v207, -v38 row_newbcast:4 row_mask:0xf bank_mask:0xf
	v_fmac_f32_dpp v208, v208, -v38 row_newbcast:4 row_mask:0xf bank_mask:0xf
	v_fmac_f32_dpp v209, v209, -v38 row_newbcast:4 row_mask:0xf bank_mask:0xf
	v_fmac_f32_dpp v206, v206, -v39 row_newbcast:5 row_mask:0xf bank_mask:0xf
	v_fmac_f32_dpp v207, v207, -v39 row_newbcast:5 row_mask:0xf bank_mask:0xf
	v_fmac_f32_dpp v208, v208, -v39 row_newbcast:5 row_mask:0xf bank_mask:0xf
	v_fmac_f32_dpp v209, v209, -v39 row_newbcast:5 row_mask:0xf bank_mask:0xf
	v_fmac_f32_dpp v206, v206, -v40 row_newbcast:6 row_mask:0xf bank_mask:0xf
	v_fmac_f32_dpp v207, v207, -v40 row_newbcast:6 row_mask:0xf bank_mask:0xf
	v_fmac_f32_dpp v208, v208, -v40 row_newbcast:6 row_mask:0xf bank_mask:0xf
	v_fmac_f32_dpp v209, v209, -v40 row_newbcast:6 row_mask:0xf bank_mask:0xf
	v_fmac_f32_dpp v206, v206, -v41 row_newbcast:7 row_mask:0xf bank_mask:0xf
	v_fmac_f32_dpp v207, v207, -v41 row_newbcast:7 row_mask:0xf bank_mask:0xf
	v_fmac_f32_dpp v208, v208, -v41 row_newbcast:7 row_mask:0xf bank_mask:0xf
	v_fmac_f32_dpp v209, v209, -v41 row_newbcast:7 row_mask:0xf bank_mask:0xf
	v_fmac_f32_dpp v206, v206, -v42 row_newbcast:8 row_mask:0xf bank_mask:0xf
	v_fmac_f32_dpp v207, v207, -v42 row_newbcast:8 row_mask:0xf bank_mask:0xf
	v_fmac_f32_dpp v208, v208, -v42 row_newbcast:8 row_mask:0xf bank_mask:0xf
	v_fmac_f32_dpp v209, v209, -v42 row_newbcast:8 row_mask:0xf bank_mask:0xf
	v_fmac_f32_dpp v206, v206, -v43 row_newbcast:9 row_mask:0xf bank_mask:0xf
	v_fmac_f32_dpp v207, v207, -v43 row_newbcast:9 row_mask:0xf bank_mask:0xf
	v_fmac_f32_dpp v208, v208, -v43 row_newbcast:9 row_mask:0xf bank_mask:0xf
	v_fmac_f32_dpp v209, v209, -v43 row_newbcast:9 row_mask:0xf bank_mask:0xf
	v_fmac_f32_dpp v206, v206, -v44 row_newbcast:10 row_mask:0xf bank_mask:0xf
	v_fmac_f32_dpp v207, v207, -v44 row_newbcast:10 row_mask:0xf bank_mask:0xf
	v_fmac_f32_dpp v208, v208, -v44 row_newbcast:10 row_mask:0xf bank_mask:0xf
	v_fmac_f32_dpp v209, v209, -v44 row_newbcast:10 row_mask:0xf bank_mask:0xf
	v_fmac_f32_dpp v206, v206, -v45 row_newbcast:11 row_mask:0xf bank_mask:0xf
	v_fmac_f32_dpp v207, v207, -v45 row_newbcast:11 row_mask:0xf bank_mask:0xf
	v_fmac_f32_dpp v208, v208, -v45 row_newbcast:11 row_mask:0xf bank_mask:0xf
	v_fmac_f32_dpp v209, v209, -v45 row_newbcast:11 row_mask:0xf bank_mask:0xf
	v_fmac_f32_dpp v206, v206, -v46 row_newbcast:12 row_mask:0xf bank_mask:0xf
	v_fmac_f32_dpp v207, v207, -v46 row_newbcast:12 row_mask:0xf bank_mask:0xf
	v_fmac_f32_dpp v208, v208, -v46 row_newbcast:12 row_mask:0xf bank_mask:0xf
	v_fmac_f32_dpp v209, v209, -v46 row_newbcast:12 row_mask:0xf bank_mask:0xf
	v_fmac_f32_dpp v206, v206, -v47 row_newbcast:13 row_mask:0xf bank_mask:0xf
	v_fmac_f32_dpp v207, v207, -v47 row_newbcast:13 row_mask:0xf bank_mask:0xf
	v_fmac_f32_dpp v208, v208, -v47 row_newbcast:13 row_mask:0xf bank_mask:0xf
	v_fmac_f32_dpp v209, v209, -v47 row_newbcast:13 row_mask:0xf bank_mask:0xf
	v_fmac_f32_dpp v206, v206, -v48 row_newbcast:14 row_mask:0xf bank_mask:0xf
	v_fmac_f32_dpp v207, v207, -v48 row_newbcast:14 row_mask:0xf bank_mask:0xf
	v_fmac_f32_dpp v208, v208, -v48 row_newbcast:14 row_mask:0xf bank_mask:0xf
	v_fmac_f32_dpp v209, v209, -v48 row_newbcast:14 row_mask:0xf bank_mask:0xf
	v_cvt_pk_bf16_f32 v206, v206, v207
	v_cvt_pk_bf16_f32 v207, v208, v209
	ds_write_b64 v194, v[206:207] offset:1920
	s_mov_b64 s[76:77], exec

.LBB0_1147:
	s_andn2_b64 vcc, exec, s[76:77]
	s_cbranch_vccnz .LBB0_1160
	s_setprio 3
	s_waitcnt vmcnt(6)
	v_add_u32_e32 v34, v125, v132
	v_add_u32_e32 v35, v125, v133
	ds_write_b128 v34, v[82:85]
	ds_write_b128 v35, v[78:81]
	ds_write_b128 v34, v[90:93] offset:4608
	ds_write_b128 v35, v[86:89] offset:4608
	ds_write_b128 v34, v[74:77] offset:9216
	s_waitcnt vmcnt(5)
	ds_write_b128 v35, v[70:73] offset:9216
	s_waitcnt vmcnt(4)
	ds_write_b128 v34, v[66:69] offset:13824
	s_waitcnt vmcnt(3)
	ds_write_b128 v35, v[58:61] offset:13824
	s_waitcnt vmcnt(2)
	ds_write_b128 v34, v[54:57] offset:18432
	s_waitcnt vmcnt(1)
	ds_write_b128 v35, v[50:53] offset:18432
	s_mov_b64 s[76:77], exec
	v_readlane_b32 s0, v254, 41
	v_readlane_b32 s1, v254, 42
	s_and_b64 s[0:1], s[76:77], s[0:1]
	s_mov_b64 exec, s[0:1]
	s_cbranch_execz .LBB0_1150
	s_waitcnt vmcnt(0)
	ds_write_b128 v174, v[62:65] offset:33792

.LBB0_1160:
.Lscan_join2:
	s_waitcnt lgkmcnt(0)
	s_barrier
	v_readlane_b32 s0, v255, 17
	v_readlane_b32 s1, v255, 18
	s_and_b64 vcc, exec, s[0:1]
	s_mov_b64 s[30:31], -1
	s_cbranch_vccnz .LBB0_1162
	v_readlane_b32 s0, v255, 13
	v_add_u32_e32 v246, v115, v155
	s_nop 0
	s_nop 0
	s_mul_i32 s1, s0, 0x1e00
	s_lshl_b32 s0, s0, 13
	v_add_u32_e32 v246, 0x10c00, v246
	v_add_u32_e32 v251, 0x10c00, v113
	v_add_u32_e32 v252, s1, v166
	v_add_u32_e32 v253, s0, v165
	v_add_u32_e32 v247, 0x1200, v246
	v_bfe_u32 v248, v0, 4, 2
	v_mul_u32_u24_e32 v248, 0x240, v248
	v_bfe_u32 v249, v0, 2, 2
	v_mul_u32_u24_e32 v249, 0x90, v249
	v_and_b32_e32 v250, 3, v0
	v_add_u32_e32 v248, v248, v249
	v_lshl_add_u32 v248, v250, 3, v248
	v_add_u32_e32 v248, 0x10c00, v248
	v_bfe_u32 v249, v0, 6, 2
	v_lshl_add_u32 v250, v249, 5, v248
	ds_read2_b64 v[18:21], v246 offset1:4
	ds_read2_b64 v[22:25], v246 offset0:8 offset1:12
	ds_read_b64_tr_b16 v[66:67], v250 offset:18432
	ds_read2_b64 v[68:71], v252 offset1:80
	v_cvt_pk_bf16_f32 v198, v2, v3
	v_cvt_pk_bf16_f32 v199, v4, v5
	v_cvt_pk_bf16_f32 v202, v10, v11
	v_cvt_pk_bf16_f32 v203, v12, v13
	v_cvt_pk_bf16_f32 v200, v6, v7
	v_cvt_pk_bf16_f32 v201, v8, v9
	v_cvt_pk_bf16_f32 v204, v14, v15
	v_cvt_pk_bf16_f32 v205, v16, v17
	ds_read2_b64 v[26:29], v247 offset1:4
	ds_read2_b64 v[30:33], v247 offset0:8 offset1:12
	ds_read2_b64 v[72:75], v252 offset0:160 offset1:240
	s_waitcnt lgkmcnt(6)
	v_mfma_f32_16x16x16_bf16 v[206:209], v[18:19], v[198:199], 0
	s_waitcnt lgkmcnt(5)
	v_mfma_f32_16x16x16_bf16 v[210:213], v[22:23], v[202:203], 0
	ds_read_b64_tr_b16 v[34:35], v248 offset:9216
	ds_read_b64_tr_b16 v[36:37], v248 offset:9248
	ds_read_b64_tr_b16 v[38:39], v248 offset:9280
	ds_read_b64_tr_b16 v[40:41], v248 offset:9312
	v_mfma_f32_16x16x16_bf16 v[206:209], v[20:21], v[200:201], v[206:209]
	v_mfma_f32_16x16x16_bf16 v[210:213], v[24:25], v[204:205], v[210:213]
	ds_read_b64_tr_b16 v[42:43], v248 offset:13824
	ds_read_b64_tr_b16 v[44:45], v248 offset:13856
	ds_read_b64_tr_b16 v[46:47], v248 offset:13888
	ds_read_b64_tr_b16 v[48:49], v248 offset:13920
	s_waitcnt lgkmcnt(12)
	s_waitcnt lgkmcnt(11)
	v_mfma_f32_16x16x16_bf16 v[210:213], v[68:69], v[66:67], v[210:213]
	s_waitcnt lgkmcnt(10)
	v_mfma_f32_16x16x16_bf16 v[214:217], v[26:27], v[198:199], 0
	s_waitcnt lgkmcnt(9)
	v_mfma_f32_16x16x16_bf16 v[218:221], v[30:31], v[202:203], 0
	v_mfma_f32_16x16x16_bf16 v[214:217], v[28:29], v[200:201], v[214:217]
	v_mfma_f32_16x16x16_bf16 v[218:221], v[32:33], v[204:205], v[218:221]
	ds_read_b128 v[50:53], v251 offset:33792
	ds_read_b128 v[54:57], v251 offset:33856
	ds_read_b128 v[58:61], v251 offset:33920
	ds_read_b128 v[62:65], v251 offset:33984
	v_add_u32_e32 v246, 0x900, v246
	ds_read2_b64 v[76:79], v246 offset1:4
	s_waitcnt lgkmcnt(13)
	ds_read2_b64 v[80:83], v246 offset0:8 offset1:12
	v_pk_add_f32 v[206:207], v[206:207], v[210:211]
	v_pk_add_f32 v[208:209], v[208:209], v[212:213]
	v_cvt_pk_bf16_f32 v242, v206, v207
	v_cvt_pk_bf16_f32 v243, v208, v209
	s_waitcnt lgkmcnt(13)
	ds_read_b64_tr_b16 v[84:85], v250 offset:20736
	v_add_u32_e32 v252, 0xf00, v252
	s_waitcnt lgkmcnt(13)
	ds_read2_b64 v[86:89], v252 offset1:80
	v_mfma_f32_16x16x16_bf16 v[238:241], v[74:75], v[242:243], 0
	v_mfma_f32_16x16x16_bf16 v[214:217], v[70:71], v[66:67], v[214:217]
	v_mfma_f32_16x16x16_bf16 v[2:5], v[34:35], v[66:67], v[2:5]
	v_mfma_f32_16x16x16_bf16 v[6:9], v[36:37], v[66:67], v[6:9]
	s_waitcnt lgkmcnt(12)
	v_mfma_f32_16x16x16_bf16 v[10:13], v[38:39], v[66:67], v[10:13]
	v_mfma_f32_16x16x16_bf16 v[14:17], v[40:41], v[66:67], v[14:17]
	ds_read2_b64 v[90:93], v252 offset0:160 offset1:240
	v_add_u32_e32 v247, 0x900, v247
	ds_read2_b64 v[26:29], v247 offset1:4
	s_waitcnt lgkmcnt(13)
	ds_read2_b64 v[30:33], v247 offset0:8 offset1:12
	v_cvt_pk_bf16_f32 v244, -v238, -v239
	v_cvt_pk_bf16_f32 v245, -v240, -v241
	s_waitcnt lgkmcnt(13)
	ds_read_b64_tr_b16 v[34:35], v248 offset:11520
	s_waitcnt lgkmcnt(13)
	ds_read_b64_tr_b16 v[36:37], v248 offset:11552
	s_waitcnt lgkmcnt(13)
	ds_read_b64_tr_b16 v[38:39], v248 offset:11584
	s_waitcnt lgkmcnt(13)
	ds_read_b64_tr_b16 v[40:41], v248 offset:11616
	v_mfma_f32_16x16x16_bf16 v[2:5], v[42:43], v[244:245], v[2:5]
	v_mfma_f32_16x16x16_bf16 v[6:9], v[44:45], v[244:245], v[6:9]
	v_mfma_f32_16x16x16_bf16 v[10:13], v[46:47], v[244:245], v[10:13]
	v_mfma_f32_16x16x16_bf16 v[14:17], v[48:49], v[244:245], v[14:17]
	v_mfma_f32_16x16x16_bf16 v[218:221], v[72:73], v[244:245], v[218:221]
	s_waitcnt lgkmcnt(13)
	ds_read_b64_tr_b16 v[42:43], v248 offset:16128
	s_waitcnt lgkmcnt(13)
	ds_read_b64_tr_b16 v[44:45], v248 offset:16160
	s_waitcnt lgkmcnt(13)
	ds_read_b64_tr_b16 v[46:47], v248 offset:16192
	s_waitcnt lgkmcnt(13)
	ds_read_b64_tr_b16 v[48:49], v248 offset:16224
	v_pk_mul_f32 v[2:3], v[50:51], v[2:3]
	v_pk_mul_f32 v[4:5], v[52:53], v[4:5]
	v_pk_mul_f32 v[6:7], v[54:55], v[6:7]
	v_pk_mul_f32 v[8:9], v[56:57], v[8:9]
	v_pk_mul_f32 v[10:11], v[58:59], v[10:11]
	v_pk_mul_f32 v[12:13], v[60:61], v[12:13]
	v_pk_mul_f32 v[14:15], v[62:63], v[14:15]
	v_pk_mul_f32 v[16:17], v[64:65], v[16:17]
	v_pk_add_f32 v[214:215], v[214:215], v[218:219]
	v_pk_add_f32 v[216:217], v[216:217], v[220:221]
	s_waitcnt lgkmcnt(13)
	ds_write2st64_b32 v253, v214, v215 offset0:0 offset1:1
	s_waitcnt lgkmcnt(13)
	ds_write2st64_b32 v253, v216, v217 offset0:2 offset1:3
	s_waitcnt lgkmcnt(13)
	ds_read_b128 v[50:53], v251 offset:34048
	s_waitcnt lgkmcnt(13)
	ds_read_b128 v[54:57], v251 offset:34112
	s_waitcnt lgkmcnt(13)
	ds_read_b128 v[58:61], v251 offset:34176
	s_waitcnt lgkmcnt(13)
	ds_read_b128 v[62:65], v251 offset:34240
	v_cvt_pk_bf16_f32 v198, v2, v3
	v_cvt_pk_bf16_f32 v199, v4, v5
	v_cvt_pk_bf16_f32 v202, v10, v11
	v_cvt_pk_bf16_f32 v203, v12, v13
	v_cvt_pk_bf16_f32 v200, v6, v7
	v_cvt_pk_bf16_f32 v201, v8, v9
	v_cvt_pk_bf16_f32 v204, v14, v15
	v_cvt_pk_bf16_f32 v205, v16, v17
	v_mfma_f32_16x16x16_bf16 v[206:209], v[76:77], v[198:199], 0
	v_mfma_f32_16x16x16_bf16 v[210:213], v[80:81], v[202:203], 0
	v_mfma_f32_16x16x16_bf16 v[206:209], v[78:79], v[200:201], v[206:209]
	v_mfma_f32_16x16x16_bf16 v[210:213], v[82:83], v[204:205], v[210:213]
	v_mfma_f32_16x16x16_bf16 v[210:213], v[86:87], v[84:85], v[210:213]
	v_mfma_f32_16x16x16_bf16 v[214:217], v[26:27], v[198:199], 0
	v_mfma_f32_16x16x16_bf16 v[218:221], v[30:31], v[202:203], 0
	v_mfma_f32_16x16x16_bf16 v[214:217], v[28:29], v[200:201], v[214:217]
	v_mfma_f32_16x16x16_bf16 v[218:221], v[32:33], v[204:205], v[218:221]
	s_nop 3
	v_pk_add_f32 v[206:207], v[206:207], v[210:211]
	v_pk_add_f32 v[208:209], v[208:209], v[212:213]
	v_cvt_pk_bf16_f32 v242, v206, v207
	v_cvt_pk_bf16_f32 v243, v208, v209
	s_nop 1
	v_mfma_f32_16x16x16_bf16 v[238:241], v[92:93], v[242:243], 0
	v_mfma_f32_16x16x16_bf16 v[214:217], v[88:89], v[84:85], v[214:217]
	s_waitcnt lgkmcnt(12)
	v_mfma_f32_16x16x16_bf16 v[2:5], v[34:35], v[84:85], v[2:5]
	v_mfma_f32_16x16x16_bf16 v[6:9], v[36:37], v[84:85], v[6:9]
	s_waitcnt lgkmcnt(10)
	v_mfma_f32_16x16x16_bf16 v[10:13], v[38:39], v[84:85], v[10:13]
	v_mfma_f32_16x16x16_bf16 v[14:17], v[40:41], v[84:85], v[14:17]
	s_nop 0
	v_cvt_pk_bf16_f32 v244, -v238, -v239
	v_cvt_pk_bf16_f32 v245, -v240, -v241
	s_waitcnt lgkmcnt(8)
	s_nop 0
	v_mfma_f32_16x16x16_bf16 v[2:5], v[42:43], v[244:245], v[2:5]
	v_mfma_f32_16x16x16_bf16 v[6:9], v[44:45], v[244:245], v[6:9]
	s_waitcnt lgkmcnt(6)
	v_mfma_f32_16x16x16_bf16 v[10:13], v[46:47], v[244:245], v[10:13]
	v_mfma_f32_16x16x16_bf16 v[14:17], v[48:49], v[244:245], v[14:17]
	v_mfma_f32_16x16x16_bf16 v[218:221], v[90:91], v[244:245], v[218:221]
	s_waitcnt lgkmcnt(3)
	s_nop 1
	v_pk_mul_f32 v[2:3], v[50:51], v[2:3]
	v_pk_mul_f32 v[4:5], v[52:53], v[4:5]
	s_waitcnt lgkmcnt(2)
	v_pk_mul_f32 v[6:7], v[54:55], v[6:7]
	v_pk_mul_f32 v[8:9], v[56:57], v[8:9]
	s_waitcnt lgkmcnt(1)
	v_pk_mul_f32 v[10:11], v[58:59], v[10:11]
	v_pk_mul_f32 v[12:13], v[60:61], v[12:13]
	s_waitcnt lgkmcnt(0)
	v_pk_mul_f32 v[14:15], v[62:63], v[14:15]
	v_pk_mul_f32 v[16:17], v[64:65], v[16:17]
	v_pk_add_f32 v[214:215], v[214:215], v[218:219]
	v_pk_add_f32 v[216:217], v[216:217], v[220:221]
	ds_write2st64_b32 v253, v214, v215 offset0:16 offset1:17
	ds_write2st64_b32 v253, v216, v217 offset0:18 offset1:19
	v_mov_b64_e32 v[18:19], v[2:3]
	v_mov_b64_e32 v[20:21], v[4:5]
	v_mov_b64_e32 v[22:23], v[6:7]
	v_mov_b64_e32 v[24:25], v[8:9]
	v_mov_b64_e32 v[26:27], v[10:11]
	v_mov_b64_e32 v[28:29], v[12:13]
	v_mov_b64_e32 v[30:31], v[14:15]
	v_mov_b64_e32 v[32:33], v[16:17]
	s_branch .Lscan_join3
.LBB0_1162:
	s_andn2_b64 vcc, exec, s[30:31]
	s_cbranch_vccnz .LBB0_1185
	v_readlane_b32 s0, v255, 13
	s_cmp_lg_u32 s16, s0
	s_mov_b64 s[30:31], -1
	s_cbranch_scc0 .LBB0_1169
	v_readlane_b32 s0, v255, 11
	s_cmpk_gt_u32 s0, 0x44
	s_cbranch_scc1 .LBB0_1168
	s_setprio 3
	v_writelane_b32 v255, s4, 24
	ds_read_b128 v[2:5], v179 offset:0
	ds_read_b128 v[10:13], v179 offset:13824
	ds_read_b128 v[6:9], v179 offset:64
	ds_read_b128 v[14:17], v179 offset:13888
	v_readlane_b32 s0, v255, 13
	v_readlane_b32 s2, v254, 55
	v_readlane_b32 s3, v254, 56
	v_readlane_b32 s4, v254, 57
	v_readlane_b32 s5, v254, 58
	v_readlane_b32 s6, v254, 63
	v_readlane_b32 s7, v255, 0
	s_xor_b32 s0, s0, 1
	s_mulk_i32 s0, 0x1e00
	v_readlane_b32 s8, v255, 1
	v_readlane_b32 s9, v255, 2
	v_readlane_b32 s10, v255, 3
	v_readlane_b32 s11, v255, 4
	v_and_b32_e32 v42, 15, v0
	v_bfe_u32 v43, v0, 4, 2
	v_mad_u32_u24 v46, v42, 38, v114
	v_lshl_add_u32 v46, v43, 3, v46
	v_add_u32_e32 v46, s0, v46
	v_mad_u32_u24 v47, v42, 40, v46
	v_lshl_add_u32 v47, v43, 3, v47
	s_waitcnt lgkmcnt(2)
	v_mfma_f32_16x16x32_bf16 v[34:37], v[10:13], v[2:5], 0
	s_waitcnt lgkmcnt(0)
	v_mfma_f32_16x16x32_bf16 v[34:37], v[14:17], v[6:9], v[34:37]
	ds_read_b128 v[10:13], v179 offset:9216
	ds_read_b128 v[14:17], v179 offset:9280
	v_cndmask_b32_e64 v44, 0, 1.0, s[6:7]
	v_cndmask_b32_e64 v45, 0, 1.0, s[8:9]
	v_cndmask_b32_e64 v42, 1.0, 0, s[2:3]
	v_cndmask_b32_e64 v43, 0, 1.0, s[4:5]
	v_cndmask_b32_e64 v44, v44, 0, s[8:9]
	v_cndmask_b32_e64 v45, v45, 0, s[10:11]
	v_cndmask_b32_e64 v42, v42, 0, s[4:5]
	v_cndmask_b32_e64 v43, v43, 0, s[6:7]
	v_cndmask_b32_e64 v34, 0, v34, s[4:5]
	v_cndmask_b32_e64 v35, 0, v35, s[6:7]
	v_cndmask_b32_e64 v36, 0, v36, s[8:9]
	v_cndmask_b32_e64 v37, 0, v37, s[10:11]
	ds_write_b128 v47, v[34:37] offset:2560
	s_waitcnt lgkmcnt(1)
	v_mfma_f32_16x16x32_bf16 v[38:41], v[10:13], v[2:5], 0
	v_mfma_f32_16x16x32_bf16 v[38:41], v[14:17], v[6:9], v[38:41]
	ds_read_b128 v[2:5], v179 offset:4608
	ds_read_b128 v[6:9], v179 offset:4672
	v_bfe_u32 v34, v0, 4, 2
	v_lshlrev_b32_e32 v34, 4, v34
	v_sub_u32_e32 v47, v47, v34
	s_nop 4
	v_cndmask_b32_e64 v38, 0, v38, s[4:5]
	v_cndmask_b32_e64 v39, 0, v39, s[6:7]
	v_cndmask_b32_e64 v40, 0, v40, s[8:9]
	v_cndmask_b32_e64 v41, 0, v41, s[10:11]
	v_cvt_pk_bf16_f32 v38, v38, v39
	v_cvt_pk_bf16_f32 v39, v40, v41
	ds_write_b64 v46, v[38:39]
	s_waitcnt lgkmcnt(1)
	v_mfma_f32_16x16x32_bf16 v[34:37], v[10:13], v[2:5], 0
	v_mfma_f32_16x16x32_bf16 v[34:37], v[14:17], v[6:9], v[34:37]
	ds_read_b128 v[10:13], v179 offset:13824
	ds_read_b128 v[14:17], v179 offset:13888
	s_waitcnt lgkmcnt(0)
	v_mfma_f32_16x16x32_bf16 v[38:41], v[10:13], v[2:5], 0
	v_mfma_f32_16x16x32_bf16 v[38:41], v[14:17], v[6:9], v[38:41]
	ds_read_b128 v[2:5], v47 offset:2560
	ds_read_b128 v[6:9], v47 offset:2576
	ds_read_b128 v[10:13], v47 offset:2592
	ds_read_b128 v[14:17], v47 offset:2608
	v_cndmask_b32_e64 v34, v34, 0, s[2:3]
	v_cndmask_b32_e64 v35, 0, v35, s[4:5]
	v_cndmask_b32_e64 v36, 0, v36, s[6:7]
	v_cndmask_b32_e64 v37, 0, v37, s[8:9]
	v_cvt_pk_bf16_f32 v34, v34, v35
	v_cvt_pk_bf16_f32 v35, v36, v37
	ds_write_b64 v46, v[34:35] offset:640
	v_cndmask_b32_e64 v38, v38, 0, s[2:3]
	v_cndmask_b32_e64 v39, 0, v39, s[4:5]
	v_cndmask_b32_e64 v40, 0, v40, s[6:7]
	v_cndmask_b32_e64 v41, 0, v41, s[8:9]
	v_cvt_pk_bf16_f32 v38, v38, v39
	v_cvt_pk_bf16_f32 v39, v40, v41
	ds_write_b64 v46, v[38:39] offset:1280
	s_waitcnt lgkmcnt(2)
	v_fmac_f32_dpp v42, v42, -v2 row_newbcast:0 row_mask:0xf bank_mask:0xf
	s_nop 1
	v_fmac_f32_dpp v42, v42, -v3 row_newbcast:1 row_mask:0xf bank_mask:0xf
	v_fmac_f32_dpp v43, v43, -v3 row_newbcast:1 row_mask:0xf bank_mask:0xf
	s_nop 0
	v_fmac_f32_dpp v42, v42, -v4 row_newbcast:2 row_mask:0xf bank_mask:0xf
	v_fmac_f32_dpp v43, v43, -v4 row_newbcast:2 row_mask:0xf bank_mask:0xf
	v_fmac_f32_dpp v44, v44, -v4 row_newbcast:2 row_mask:0xf bank_mask:0xf
	v_fmac_f32_dpp v42, v42, -v5 row_newbcast:3 row_mask:0xf bank_mask:0xf
	v_fmac_f32_dpp v43, v43, -v5 row_newbcast:3 row_mask:0xf bank_mask:0xf
	v_fmac_f32_dpp v44, v44, -v5 row_newbcast:3 row_mask:0xf bank_mask:0xf
	v_fmac_f32_dpp v45, v45, -v5 row_newbcast:3 row_mask:0xf bank_mask:0xf
	v_fmac_f32_dpp v42, v42, -v6 row_newbcast:4 row_mask:0xf bank_mask:0xf
	v_fmac_f32_dpp v43, v43, -v6 row_newbcast:4 row_mask:0xf bank_mask:0xf
	v_fmac_f32_dpp v44, v44, -v6 row_newbcast:4 row_mask:0xf bank_mask:0xf
	v_fmac_f32_dpp v45, v45, -v6 row_newbcast:4 row_mask:0xf bank_mask:0xf
	v_fmac_f32_dpp v42, v42, -v7 row_newbcast:5 row_mask:0xf bank_mask:0xf
	v_fmac_f32_dpp v43, v43, -v7 row_newbcast:5 row_mask:0xf bank_mask:0xf
	v_fmac_f32_dpp v44, v44, -v7 row_newbcast:5 row_mask:0xf bank_mask:0xf
	v_fmac_f32_dpp v45, v45, -v7 row_newbcast:5 row_mask:0xf bank_mask:0xf
	v_fmac_f32_dpp v42, v42, -v8 row_newbcast:6 row_mask:0xf bank_mask:0xf
	v_fmac_f32_dpp v43, v43, -v8 row_newbcast:6 row_mask:0xf bank_mask:0xf
	v_fmac_f32_dpp v44, v44, -v8 row_newbcast:6 row_mask:0xf bank_mask:0xf
	v_fmac_f32_dpp v45, v45, -v8 row_newbcast:6 row_mask:0xf bank_mask:0xf
	v_fmac_f32_dpp v42, v42, -v9 row_newbcast:7 row_mask:0xf bank_mask:0xf
	v_fmac_f32_dpp v43, v43, -v9 row_newbcast:7 row_mask:0xf bank_mask:0xf
	v_fmac_f32_dpp v44, v44, -v9 row_newbcast:7 row_mask:0xf bank_mask:0xf
	v_fmac_f32_dpp v45, v45, -v9 row_newbcast:7 row_mask:0xf bank_mask:0xf
	v_fmac_f32_dpp v42, v42, -v10 row_newbcast:8 row_mask:0xf bank_mask:0xf
	v_fmac_f32_dpp v43, v43, -v10 row_newbcast:8 row_mask:0xf bank_mask:0xf
	v_fmac_f32_dpp v44, v44, -v10 row_newbcast:8 row_mask:0xf bank_mask:0xf
	v_fmac_f32_dpp v45, v45, -v10 row_newbcast:8 row_mask:0xf bank_mask:0xf
	v_fmac_f32_dpp v42, v42, -v11 row_newbcast:9 row_mask:0xf bank_mask:0xf
	v_fmac_f32_dpp v43, v43, -v11 row_newbcast:9 row_mask:0xf bank_mask:0xf
	v_fmac_f32_dpp v44, v44, -v11 row_newbcast:9 row_mask:0xf bank_mask:0xf
	v_fmac_f32_dpp v45, v45, -v11 row_newbcast:9 row_mask:0xf bank_mask:0xf
	v_fmac_f32_dpp v42, v42, -v12 row_newbcast:10 row_mask:0xf bank_mask:0xf
	v_fmac_f32_dpp v43, v43, -v12 row_newbcast:10 row_mask:0xf bank_mask:0xf
	v_fmac_f32_dpp v44, v44, -v12 row_newbcast:10 row_mask:0xf bank_mask:0xf
	v_fmac_f32_dpp v45, v45, -v12 row_newbcast:10 row_mask:0xf bank_mask:0xf
	v_fmac_f32_dpp v42, v42, -v13 row_newbcast:11 row_mask:0xf bank_mask:0xf
	v_fmac_f32_dpp v43, v43, -v13 row_newbcast:11 row_mask:0xf bank_mask:0xf
	v_fmac_f32_dpp v44, v44, -v13 row_newbcast:11 row_mask:0xf bank_mask:0xf
	v_fmac_f32_dpp v45, v45, -v13 row_newbcast:11 row_mask:0xf bank_mask:0xf
	v_fmac_f32_dpp v42, v42, -v14 row_newbcast:12 row_mask:0xf bank_mask:0xf
	v_fmac_f32_dpp v43, v43, -v14 row_newbcast:12 row_mask:0xf bank_mask:0xf
	v_fmac_f32_dpp v44, v44, -v14 row_newbcast:12 row_mask:0xf bank_mask:0xf
	v_fmac_f32_dpp v45, v45, -v14 row_newbcast:12 row_mask:0xf bank_mask:0xf
	v_fmac_f32_dpp v42, v42, -v15 row_newbcast:13 row_mask:0xf bank_mask:0xf
	v_fmac_f32_dpp v43, v43, -v15 row_newbcast:13 row_mask:0xf bank_mask:0xf
	v_fmac_f32_dpp v44, v44, -v15 row_newbcast:13 row_mask:0xf bank_mask:0xf
	v_fmac_f32_dpp v45, v45, -v15 row_newbcast:13 row_mask:0xf bank_mask:0xf
	v_fmac_f32_dpp v42, v42, -v16 row_newbcast:14 row_mask:0xf bank_mask:0xf
	v_fmac_f32_dpp v43, v43, -v16 row_newbcast:14 row_mask:0xf bank_mask:0xf
	v_fmac_f32_dpp v44, v44, -v16 row_newbcast:14 row_mask:0xf bank_mask:0xf
	v_fmac_f32_dpp v45, v45, -v16 row_newbcast:14 row_mask:0xf bank_mask:0xf
	v_cvt_pk_bf16_f32 v42, v42, v43
	v_cvt_pk_bf16_f32 v43, v44, v45
	ds_write_b64 v46, v[42:43] offset:1920
	s_mov_b64 s[30:31], exec

.LBB0_1169:
	s_andn2_b64 vcc, exec, s[30:31]
	s_cbranch_vccnz .LBB0_1186
	s_setprio 3
	s_waitcnt vmcnt(6)
	v_add_u32_e32 v2, v125, v132
	v_add_u32_e32 v3, v125, v133
	ds_write_b128 v2, v[82:85] offset:34304
	ds_write_b128 v3, v[78:81] offset:34304
	ds_write_b128 v2, v[90:93] offset:38912
	ds_write_b128 v3, v[86:89] offset:38912
	ds_write_b128 v2, v[74:77] offset:43520
	s_waitcnt vmcnt(5)
	ds_write_b128 v3, v[70:73] offset:43520
	s_waitcnt vmcnt(4)
	ds_write_b128 v2, v[66:69] offset:48128
	s_waitcnt vmcnt(3)
	ds_write_b128 v3, v[58:61] offset:48128
	s_waitcnt vmcnt(2)
	ds_write_b128 v2, v[54:57] offset:52736
	s_waitcnt vmcnt(1)
	ds_write_b128 v3, v[50:53] offset:52736
	s_mov_b64 s[30:31], exec
	v_readlane_b32 s0, v254, 41
	v_readlane_b32 s1, v254, 42
	s_and_b64 s[0:1], s[30:31], s[0:1]
	s_mov_b64 exec, s[0:1]
	s_cbranch_execz .LBB0_1172
	s_waitcnt vmcnt(0)
	ds_write_b128 v177, v[62:65]

.LBB0_1190:
	s_setprio 0
	v_readlane_b32 s4, v254, 2
	v_readlane_b32 s5, v254, 3
	v_readlane_b32 s2, v254, 33
	s_waitcnt lgkmcnt(0)
	s_barrier
